# stack10 + GEMM phase prologues: K-tile 1 LDS-DMA loads issued before K-tile 0's wait (vmcnt(2)+barrier -> vmcnt(8)+barrier after them), both round trips overlap
# baseline (speedup 1.0000x reference)
; #define PG8_STAGE(bufoff, gbase, voff) do { _Pragma("unroll") for (int _i = 0; _i < 2; ++_i) \
;         __builtin_amdgcn_global_load_lds((const unsigned*)((const char*)(gbase) + (voff)[_i]), (PG8_LAS unsigned*)(lds + (bufoff) + ldsw + _i * 8192), 16, 0, 0); } while (0)
; #define PG8_WAIT_V(n) asm volatile("s_waitcnt vmcnt(" #n ")" ::: "memory")
; #define PG8_BAR __builtin_amdgcn_s_barrier()
; template <class Epi, class Sched, bool ALIGN_EPI = false, bool SP2 = false>
; __device__ __forceinline__ void gemm_phase(PG8_LAS unsigned char* lds, const Gemm g, const Sched& S, const Epi& E, Stopwatch& sw) {
;     ...
;         PG8_STAGE(PG8_SB(0, 0), cB, voffB); PG8_STAGE(PG8_SB(0, 1), cB + hstep, voffB); PG8_STAGE(PG8_SA(0, 0), cA, voffA); PG8_STAGE(PG8_SA(0, 1), cA + hstep, voffA);
;         if (wr == 1) PG8_BAR;
;         PG8_WAIT_V(2); PG8_BAR;
;         PG8_STAGE(PG8_SB(1, 0), cB + kstep, voffB); PG8_STAGE(PG8_SA(1, 0), cA + kstep, voffA); PG8_STAGE(PG8_SB(1, 1), cB + hstep + kstep, voffB);
;         PG8_WAIT_V(6); PG8_BAR;
.LBB0_147:
	v_lshrrev_b32_e32 v20, 1, v14
	v_and_b32_e32 v20, 24, v20
	v_and_b32_e32 v15, 15, v14
	v_lshlrev_b32_e32 v21, 1, v20
	v_lshlrev_b32_e32 v14, 2, v14
	s_lshl_b32 s3, s3, 5
	v_lshl_or_b32 v1, s5, 6, v15
	v_lshl_or_b32 v15, v15, 6, v21
	s_lshl_b32 s5, s5, 13
	v_and_b32_e32 v14, 32, v14
	s_and_b32 s3, s3, 0x60
	v_bitop3_b32 v21, v15, s5, v14 bitop3:0xde
	s_lshl_b32 s5, s3, 7
	s_mul_i32 s34, s31, 0x3800
	v_bitop3_b32 v14, v15, s5, v14 bitop3:0xde
	s_lshl_b64 s[24:25], s[34:35], 2
	v_readlane_b32 s5, v250, 30
	s_add_u32 s44, s5, s24
	v_readlane_b32 s5, v250, 31
	v_readlane_b32 s56, v253, 57
	s_addc_u32 s45, s5, s25
	s_add_i32 s5, s81, 0x18000
	v_mov_b32_e32 v205, v3
	v_readlane_b32 s57, v253, 58
	v_lshl_add_u64 v[4:5], v[4:5], 0, s[20:21]
	s_mov_b32 m0, s5
	s_add_i32 s34, s81, 0x1a000
	v_lshl_add_u64 v[16:17], s[56:57], 0, v[204:205]
	v_mov_b32_e32 v203, v3
	global_load_lds_dwordx4 v[4:5], off
	v_lshl_add_u64 v[4:5], v[6:7], 0, s[20:21]
	s_mov_b32 m0, s34
	s_add_i32 s40, s81, 0x8000
	s_add_i32 s41, s81, 0xa000
	v_lshl_add_u64 v[18:19], s[56:57], 0, v[202:203]
	global_load_lds_dwordx4 v[4:5], off
	v_lshl_add_u64 v[4:5], v[16:17], 0, s[20:21]
	s_mov_b32 m0, s40
	s_add_u32 s36, s38, 0x40080
	global_load_lds_dwordx4 v[4:5], off
	v_lshl_add_u64 v[4:5], v[18:19], 0, s[20:21]
	s_mov_b32 m0, s41
	s_addc_u32 s37, s39, 0
	s_add_i32 s25, s81, 0x1c000
	global_load_lds_dwordx4 v[4:5], off
	v_lshl_add_u64 v[4:5], s[36:37], 0, v[2:3]
	s_mov_b32 m0, s25
	s_add_i32 s94, s81, 0x1e000
	global_load_lds_dwordx4 v[4:5], off
	v_lshl_add_u64 v[4:5], s[36:37], 0, v[196:197]
	s_mov_b32 m0, s94
	s_cmpk_lt_u32 s0, 0x100
	global_load_lds_dwordx4 v[4:5], off
	s_waitcnt vmcnt(8)
	s_barrier
	v_lshlrev_b32_e32 v4, 14, v12
	v_and_b32_e32 v4, 0xffff8000, v4
	v_lshl_add_u32 v4, v11, 11, v4
	v_and_b32_e32 v5, 1, v12
	v_lshl_or_b32 v4, v5, 6, v4
	v_lshl_add_u32 v206, v13, 1, v4
	v_lshlrev_b32_e32 v4, 14, v8
	v_and_b32_e32 v4, 0xffff8000, v4
	s_waitcnt vmcnt(6)
	v_lshl_add_u32 v4, v9, 11, v4
	v_and_b32_e32 v5, 1, v8
	v_lshl_or_b32 v4, v5, 6, v4
	v_add_u32_e32 v227, 0, v14
	v_readlane_b32 s36, v253, 55
	s_cselect_b64 s[46:47], -1, 0
	v_or_b32_e32 v226, s3, v20
	v_mov_b32_e32 v207, v3
	v_lshl_add_u32 v208, v10, 1, v4
	v_mov_b32_e32 v209, v3
	s_mov_b32 s0, 0
	v_add_u32_e32 v228, 0x10000, v227
	v_add_u32_e32 v229, 0x14000, v227
	v_add_u32_e32 v230, 0, v21
	v_readlane_b32 s31, v253, 48
	s_mov_b32 s24, s36
	s_movk_i32 s83, 0x1c1
	s_barrier
	v_readlane_b32 s37, v253, 56
	s_branch .LBB0_150

; #define PG8_STAGE(bufoff, gbase, voff) do { _Pragma("unroll") for (int _i = 0; _i < 2; ++_i) \
;         __builtin_amdgcn_global_load_lds((const unsigned*)((const char*)(gbase) + (voff)[_i]), (PG8_LAS unsigned*)(lds + (bufoff) + ldsw + _i * 8192), 16, 0, 0); } while (0)
; #define PG8_WAIT_V(n) asm volatile("s_waitcnt vmcnt(" #n ")" ::: "memory")
; #define PG8_BAR __builtin_amdgcn_s_barrier()
; template <class Epi, class Sched, bool ALIGN_EPI = false, bool SP2 = false>
; __device__ __forceinline__ void gemm_phase(PG8_LAS unsigned char* lds, const Gemm g, const Sched& S, const Epi& E, Stopwatch& sw) {
;     ...
;         PG8_STAGE(PG8_SB(0, 0), cB, voffB); PG8_STAGE(PG8_SB(0, 1), cB + hstep, voffB); PG8_STAGE(PG8_SA(0, 0), cA, voffA); PG8_STAGE(PG8_SA(0, 1), cA + hstep, voffA);
;         if (wr == 1) PG8_BAR;
;         PG8_WAIT_V(2); PG8_BAR;
;         PG8_STAGE(PG8_SB(1, 0), cB + kstep, voffB); PG8_STAGE(PG8_SA(1, 0), cA + kstep, voffA); PG8_STAGE(PG8_SB(1, 1), cB + hstep + kstep, voffB);
;         PG8_WAIT_V(6); PG8_BAR;
.LBB0_757:
	v_mov_b32_e32 v207, v3
	v_lshl_add_u64 v[12:13], s[42:43], 0, v[206:207]
	v_mov_b32_e32 v203, v3
	v_readlane_b32 s54, v253, 63
	s_lshl_b32 s24, s24, 5
	s_add_i32 s79, s18, 0x18000
	v_lshl_add_u64 v[14:15], s[42:43], 0, v[202:203]
	v_mov_b32_e32 v209, v3
	v_readlane_b32 s55, v254, 0
	s_and_b32 s24, s24, 0x60
	v_lshl_add_u64 v[12:13], v[12:13], 0, s[20:21]
	s_mov_b32 m0, s79
	s_add_i32 s80, s18, 0x1a000
	v_lshl_add_u64 v[16:17], s[54:55], 0, v[208:209]
	v_mov_b32_e32 v205, v3
	s_lshl_b32 s31, s3, 13
	s_lshl_b32 s34, s24, 7
	global_load_lds_dwordx4 v[12:13], off
	v_lshl_add_u64 v[12:13], v[14:15], 0, s[20:21]
	s_mov_b32 m0, s80
	s_add_i32 s81, s18, 0x8000
	s_add_i32 s90, s18, 0xa000
	v_lshl_add_u64 v[18:19], s[54:55], 0, v[204:205]
	global_load_lds_dwordx4 v[12:13], off
	v_lshl_add_u64 v[12:13], v[16:17], 0, s[20:21]
	s_mov_b32 m0, s81
	s_add_u32 s36, s42, 0xc0080
	global_load_lds_dwordx4 v[12:13], off
	v_lshl_add_u64 v[12:13], v[18:19], 0, s[20:21]
	s_mov_b32 m0, s90
	s_addc_u32 s37, s43, 0
	s_add_i32 s94, s18, 0x1c000
	global_load_lds_dwordx4 v[12:13], off
	v_lshl_add_u64 v[12:13], s[36:37], 0, v[206:207]
	s_mov_b32 m0, s94
	s_add_i32 s95, s18, 0x1e000
	global_load_lds_dwordx4 v[12:13], off
	v_lshl_add_u64 v[12:13], s[36:37], 0, v[202:203]
	s_mov_b32 m0, s95
	s_cmpk_lt_u32 s0, 0x100
	global_load_lds_dwordx4 v[12:13], off
	s_waitcnt vmcnt(8)
	s_barrier
	v_lshrrev_b32_e32 v13, 1, v2
	v_and_b32_e32 v13, 24, v13
	v_and_b32_e32 v12, 15, v2
	v_lshlrev_b32_e32 v14, 1, v13
	v_lshlrev_b32_e32 v2, 2, v2
	v_lshl_or_b32 v1, s3, 6, v12
	v_lshl_or_b32 v12, v12, 6, v14
	v_and_b32_e32 v2, 32, v2
	s_movk_i32 s3, 0xc00
	v_bitop3_b32 v14, v12, s31, v2 bitop3:0xde
	v_bitop3_b32 v12, v12, s34, v2 bitop3:0xde
	v_lshrrev_b32_e32 v9, 1, v9
	v_mul_lo_u32 v2, v8, s3
	s_mov_b32 s0, 0xc000
	v_mad_u64_u32 v[8:9], s[36:37], v9, s0, v[2:3]
	v_or_b32_e32 v2, v8, v10
	v_add_lshl_u32 v210, v2, v11, 1
	v_lshrrev_b32_e32 v4, 1, v4
	v_mul_lo_u32 v2, v5, s3
	s_waitcnt vmcnt(6)
	v_mad_u64_u32 v[4:5], s[36:37], v4, s0, v[2:3]
	v_or_b32_e32 v2, v4, v6
	v_readlane_b32 s36, v254, 21
	v_readlane_b32 s76, v253, 21
	s_cselect_b64 s[48:49], -1, 0
	v_or_b32_e32 v247, s24, v13
	v_mov_b32_e32 v211, v3
	v_add_lshl_u32 v212, v2, v7, 1
	v_mov_b32_e32 v213, v3
	s_mov_b32 s0, 0
	v_add_u32_e32 v248, 0, v12
	v_add_u32_e32 v249, 0, v14
	v_readlane_b32 s3, v253, 53
	v_readlane_b32 s37, v254, 22
	s_mov_b32 s24, s36
	v_readlane_b32 s77, v253, 22
	s_barrier
	s_branch .LBB0_760

; #define PG8_STAGE(bufoff, gbase, voff) do { _Pragma("unroll") for (int _i = 0; _i < 2; ++_i) \
;         __builtin_amdgcn_global_load_lds((const unsigned*)((const char*)(gbase) + (voff)[_i]), (PG8_LAS unsigned*)(lds + (bufoff) + ldsw + _i * 8192), 16, 0, 0); } while (0)
; #define PG8_WAIT_V(n) asm volatile("s_waitcnt vmcnt(" #n ")" ::: "memory")
; #define PG8_BAR __builtin_amdgcn_s_barrier()
; template <class Epi, class Sched, bool ALIGN_EPI = false, bool SP2 = false>
; __device__ __forceinline__ void gemm_phase(PG8_LAS unsigned char* lds, const Gemm g, const Sched& S, const Epi& E, Stopwatch& sw) {
;     ...
;         PG8_STAGE(PG8_SB(0, 0), cB, voffB); PG8_STAGE(PG8_SB(0, 1), cB + hstep, voffB); PG8_STAGE(PG8_SA(0, 0), cA, voffA); PG8_STAGE(PG8_SA(0, 1), cA + hstep, voffA);
;         if (wr == 1) PG8_BAR;
;         PG8_WAIT_V(2); PG8_BAR;
;         PG8_STAGE(PG8_SB(1, 0), cB + kstep, voffB); PG8_STAGE(PG8_SA(1, 0), cA + kstep, voffA); PG8_STAGE(PG8_SB(1, 1), cB + hstep + kstep, voffB);
;         PG8_WAIT_V(6); PG8_BAR;
.LBB0_879:
	v_lshl_add_u64 v[12:13], s[42:43], 0, v[2:3]
	v_mov_b32_e32 v197, v3
	v_readlane_b32 s58, v254, 5
	s_add_i32 s73, s16, 0x18000
	v_lshl_add_u64 v[14:15], s[42:43], 0, v[196:197]
	v_mov_b32_e32 v205, v3
	v_readlane_b32 s59, v254, 6
	s_and_b32 s72, s34, 3
	v_lshl_add_u64 v[12:13], v[12:13], 0, s[20:21]
	s_mov_b32 m0, s73
	s_add_i32 s80, s16, 0x1a000
	v_lshl_add_u64 v[16:17], s[58:59], 0, v[204:205]
	v_mov_b32_e32 v203, v3
	s_lshl_b32 s34, s3, 13
	s_lshl_b32 s40, s72, 12
	global_load_lds_dwordx4 v[12:13], off
	v_lshl_add_u64 v[12:13], v[14:15], 0, s[20:21]
	s_mov_b32 m0, s80
	s_add_i32 s81, s16, 0x8000
	s_add_i32 s82, s16, 0xa000
	v_lshl_add_u64 v[18:19], s[58:59], 0, v[202:203]
	global_load_lds_dwordx4 v[12:13], off
	v_lshl_add_u64 v[12:13], v[16:17], 0, s[20:21]
	s_mov_b32 m0, s81
	s_add_u32 s38, s42, 0x80080
	global_load_lds_dwordx4 v[12:13], off
	v_lshl_add_u64 v[12:13], v[18:19], 0, s[20:21]
	s_mov_b32 m0, s82
	s_addc_u32 s39, s43, 0
	s_add_i32 s83, s16, 0x1c000
	global_load_lds_dwordx4 v[12:13], off
	v_lshl_add_u64 v[12:13], s[38:39], 0, v[2:3]
	s_mov_b32 m0, s83
	s_add_i32 s90, s16, 0x1e000
	global_load_lds_dwordx4 v[12:13], off
	v_lshl_add_u64 v[12:13], s[38:39], 0, v[196:197]
	s_mov_b32 m0, s90
	v_bfe_u32 v11, v4, 4, 2
	global_load_lds_dwordx4 v[12:13], off
	s_waitcnt vmcnt(8)
	s_barrier
	v_lshlrev_b32_e32 v13, 3, v11
	v_lshlrev_b32_e32 v14, 4, v11
	v_cmp_eq_u32_e64 s[38:39], 0, v11
	v_lshlrev_b32_e32 v11, 15, v9
	v_and_b32_e32 v11, 0xffff0000, v11
	v_lshl_add_u32 v8, v8, 12, v11
	v_and_b32_e32 v9, 1, v9
	v_lshl_or_b32 v8, v9, 6, v8
	v_lshl_add_u32 v206, v10, 1, v8
	v_lshlrev_b32_e32 v8, 15, v5
	v_and_b32_e32 v12, 15, v4
	v_lshlrev_b32_e32 v4, 2, v4
	v_and_b32_e32 v8, 0xffff0000, v8
	v_lshl_or_b32 v1, s3, 6, v12
	v_lshl_or_b32 v12, v12, 6, v14
	v_and_b32_e32 v4, 32, v4
	s_waitcnt vmcnt(6)
	v_lshl_add_u32 v6, v6, 12, v8
	v_and_b32_e32 v5, 1, v5
	v_bitop3_b32 v14, v12, s34, v4 bitop3:0xde
	v_bitop3_b32 v4, v12, s40, v4 bitop3:0xde
	s_cmpk_lt_u32 s0, 0x100
	v_lshl_or_b32 v5, v5, 6, v6
	v_readlane_b32 s40, v254, 21
	v_lshl_or_b32 v226, s72, 5, v13
	s_cselect_b64 s[48:49], -1, 0
	s_mov_b32 s0, 0
	v_mov_b32_e32 v207, v3
	v_lshl_add_u32 v208, v7, 1, v5
	v_mov_b32_e32 v209, v3
	v_add_u32_e32 v227, 0, v4
	v_add_u32_e32 v228, 0, v14
	v_readlane_b32 s34, v253, 53
	s_mov_b32 s95, s40
	s_barrier
	v_readlane_b32 s41, v254, 22
	s_waitcnt vmcnt(0)
	s_branch .LBB0_882

; #define PG8_STAGE(bufoff, gbase, voff) do { _Pragma("unroll") for (int _i = 0; _i < 2; ++_i) \
;         __builtin_amdgcn_global_load_lds((const unsigned*)((const char*)(gbase) + (voff)[_i]), (PG8_LAS unsigned*)(lds + (bufoff) + ldsw + _i * 8192), 16, 0, 0); } while (0)
; #define PG8_WAIT_V(n) asm volatile("s_waitcnt vmcnt(" #n ")" ::: "memory")
; #define PG8_BAR __builtin_amdgcn_s_barrier()
; template <class Epi, class Sched, bool ALIGN_EPI = false, bool SP2 = false>
; __device__ __forceinline__ void gemm_phase(PG8_LAS unsigned char* lds, const Gemm g, const Sched& S, const Epi& E, Stopwatch& sw) {
;     ...
;         PG8_STAGE(PG8_SB(0, 0), cB, voffB); PG8_STAGE(PG8_SB(0, 1), cB + hstep, voffB); PG8_STAGE(PG8_SA(0, 0), cA, voffA); PG8_STAGE(PG8_SA(0, 1), cA + hstep, voffA);
;         if (wr == 1) PG8_BAR;
;         PG8_WAIT_V(2); PG8_BAR;
;         PG8_STAGE(PG8_SB(1, 0), cB + kstep, voffB); PG8_STAGE(PG8_SA(1, 0), cA + kstep, voffA); PG8_STAGE(PG8_SB(1, 1), cB + hstep + kstep, voffB);
;         PG8_WAIT_V(6); PG8_BAR;
.LBB0_1107:
	v_lshrrev_b32_e32 v20, 1, v14
	v_and_b32_e32 v20, 24, v20
	v_and_b32_e32 v15, 15, v14
	v_lshlrev_b32_e32 v21, 1, v20
	v_lshlrev_b32_e32 v14, 2, v14
	s_lshl_b32 s3, s3, 5
	v_lshl_or_b32 v1, s4, 6, v15
	v_lshl_or_b32 v15, v15, 6, v21
	s_lshl_b32 s4, s4, 13
	v_and_b32_e32 v14, 32, v14
	s_and_b32 s3, s3, 0x60
	v_bitop3_b32 v21, v15, s4, v14 bitop3:0xde
	s_lshl_b32 s4, s3, 8
	v_bitop3_b32 v14, v15, s4, v14 bitop3:0xde
	v_readlane_b32 s4, v255, 26
	s_lshl_b32 s34, s4, 13
	s_lshl_b64 s[38:39], s[34:35], 2
	v_readlane_b32 s4, v250, 32
	s_add_u32 s46, s4, s38
	v_readlane_b32 s4, v250, 33
	v_readlane_b32 s58, v254, 15
	s_addc_u32 s47, s4, s39
	s_add_i32 s34, s19, 0x18000
	v_mov_b32_e32 v205, v3
	v_readlane_b32 s59, v254, 16
	v_lshl_add_u64 v[4:5], v[4:5], 0, s[20:21]
	s_mov_b32 m0, s34
	s_add_i32 s82, s19, 0x1a000
	v_lshl_add_u64 v[16:17], s[58:59], 0, v[204:205]
	v_mov_b32_e32 v203, v3
	global_load_lds_dwordx4 v[4:5], off
	v_lshl_add_u64 v[4:5], v[6:7], 0, s[20:21]
	s_mov_b32 m0, s82
	s_add_i32 s83, s19, 0x8000
	s_add_i32 s90, s19, 0xa000
	v_lshl_add_u64 v[18:19], s[58:59], 0, v[202:203]
	global_load_lds_dwordx4 v[4:5], off
	v_lshl_add_u64 v[4:5], v[16:17], 0, s[20:21]
	s_mov_b32 m0, s83
	s_add_u32 s38, s40, 0x40080
	global_load_lds_dwordx4 v[4:5], off
	v_lshl_add_u64 v[4:5], v[18:19], 0, s[20:21]
	s_mov_b32 m0, s90
	s_addc_u32 s39, s41, 0
	s_add_i32 s94, s19, 0x1c000
	global_load_lds_dwordx4 v[4:5], off
	v_lshl_add_u64 v[4:5], s[38:39], 0, v[2:3]
	s_mov_b32 m0, s94
	s_add_i32 s95, s19, 0x1e000
	global_load_lds_dwordx4 v[4:5], off
	v_lshl_add_u64 v[4:5], s[38:39], 0, v[196:197]
	s_mov_b32 m0, s95
	s_cmpk_lt_u32 s0, 0x100
	global_load_lds_dwordx4 v[4:5], off
	s_waitcnt vmcnt(8)
	s_barrier
	v_lshlrev_b32_e32 v4, 14, v12
	v_and_b32_e32 v4, 0xffff8000, v4
	v_lshl_add_u32 v4, v11, 11, v4
	v_and_b32_e32 v5, 1, v12
	v_lshl_or_b32 v4, v5, 6, v4
	v_lshl_add_u32 v206, v13, 1, v4
	v_lshlrev_b32_e32 v4, 14, v8
	v_and_b32_e32 v4, 0xffff8000, v4
	s_waitcnt vmcnt(6)
	v_lshl_add_u32 v4, v9, 11, v4
	v_and_b32_e32 v5, 1, v8
	v_lshl_or_b32 v4, v5, 6, v4
	v_readlane_b32 s38, v254, 11
	s_cselect_b64 s[48:49], -1, 0
	v_or_b32_e32 v226, s3, v20
	v_add_u32_e32 v226, s3, v226
	v_mov_b32_e32 v207, v3
	v_lshl_add_u32 v208, v10, 1, v4
	v_mov_b32_e32 v209, v3
	s_mov_b32 s0, 0
	v_add_u32_e32 v227, 0, v14
	v_add_u32_e32 v228, 0, v21
	v_readlane_b32 s31, v253, 54
	s_mov_b32 s4, s38
	s_barrier
	v_readlane_b32 s39, v254, 12
	s_branch .LBB0_1110

; #define PG8_STAGE(bufoff, gbase, voff) do { _Pragma("unroll") for (int _i = 0; _i < 2; ++_i) \
;         __builtin_amdgcn_global_load_lds((const unsigned*)((const char*)(gbase) + (voff)[_i]), (PG8_LAS unsigned*)(lds + (bufoff) + ldsw + _i * 8192), 16, 0, 0); } while (0)
; #define PG8_WAIT_V(n) asm volatile("s_waitcnt vmcnt(" #n ")" ::: "memory")
; #define PG8_BAR __builtin_amdgcn_s_barrier()
; template <class Epi, class Sched, bool ALIGN_EPI = false, bool SP2 = false>
; __device__ __forceinline__ void gemm_phase(PG8_LAS unsigned char* lds, const Gemm g, const Sched& S, const Epi& E, Stopwatch& sw) {
;     ...
;         PG8_STAGE(PG8_SB(0, 0), cB, voffB); PG8_STAGE(PG8_SB(0, 1), cB + hstep, voffB); PG8_STAGE(PG8_SA(0, 0), cA, voffA); PG8_STAGE(PG8_SA(0, 1), cA + hstep, voffA);
;         if (wr == 1) PG8_BAR;
;         PG8_WAIT_V(2); PG8_BAR;
;         PG8_STAGE(PG8_SB(1, 0), cB + kstep, voffB); PG8_STAGE(PG8_SA(1, 0), cA + kstep, voffA); PG8_STAGE(PG8_SB(1, 1), cB + hstep + kstep, voffB);
;         PG8_WAIT_V(6); PG8_BAR;
.LBB0_1217:
	v_lshl_add_u64 v[12:13], s[40:41], 0, v[2:3]
	v_mov_b32_e32 v197, v3
	s_lshl_b32 s56, s100, 22
	s_add_u32 s56, s14, s56
	s_addc_u32 s57, s15, 0
	s_add_i32 s79, s16, 0x18000
	v_lshl_add_u64 v[14:15], s[40:41], 0, v[196:197]
	v_mov_b32_e32 v205, v3
	s_and_b32 s78, s34, 3
	v_lshl_add_u64 v[12:13], v[12:13], 0, s[20:21]
	s_mov_b32 m0, s79
	s_add_i32 s80, s16, 0x1a000
	v_lshl_add_u64 v[16:17], s[56:57], 0, v[204:205]
	v_mov_b32_e32 v203, v3
	s_lshl_b32 s34, s3, 13
	s_lshl_b32 s38, s78, 12
	global_load_lds_dwordx4 v[12:13], off
	v_lshl_add_u64 v[12:13], v[14:15], 0, s[20:21]
	s_mov_b32 m0, s80
	s_add_i32 s81, s16, 0x8000
	s_add_i32 s82, s16, 0xa000
	v_lshl_add_u64 v[18:19], s[56:57], 0, v[202:203]
	global_load_lds_dwordx4 v[12:13], off
	v_lshl_add_u64 v[12:13], v[16:17], 0, s[20:21]
	s_mov_b32 m0, s81
	s_add_u32 s36, s40, 0x200080
	global_load_lds_dwordx4 v[12:13], off
	v_lshl_add_u64 v[12:13], v[18:19], 0, s[20:21]
	s_mov_b32 m0, s82
	s_addc_u32 s37, s41, 0
	s_add_i32 s83, s16, 0x1c000
	global_load_lds_dwordx4 v[12:13], off
	v_lshl_add_u64 v[12:13], s[36:37], 0, v[2:3]
	s_mov_b32 m0, s83
	s_add_i32 s90, s16, 0x1e000
	global_load_lds_dwordx4 v[12:13], off
	v_lshl_add_u64 v[12:13], s[36:37], 0, v[196:197]
	s_mov_b32 m0, s90
	v_bfe_u32 v11, v4, 4, 2
	global_load_lds_dwordx4 v[12:13], off
	s_waitcnt vmcnt(8)
	s_barrier
	v_lshlrev_b32_e32 v13, 3, v11
	v_lshlrev_b32_e32 v14, 4, v11
	v_cmp_eq_u32_e64 s[36:37], 0, v11
	v_lshlrev_b32_e32 v11, 17, v9
	v_and_b32_e32 v11, 0xfffc0000, v11
	v_lshl_add_u32 v8, v8, 14, v11
	v_and_b32_e32 v9, 1, v9
	v_lshl_or_b32 v8, v9, 6, v8
	v_lshl_add_u32 v206, v10, 1, v8
	v_lshlrev_b32_e32 v8, 17, v5
	v_and_b32_e32 v12, 15, v4
	v_lshlrev_b32_e32 v4, 2, v4
	v_and_b32_e32 v8, 0xfffc0000, v8
	v_lshl_or_b32 v1, s3, 6, v12
	v_lshl_or_b32 v12, v12, 6, v14
	v_and_b32_e32 v4, 32, v4
	s_waitcnt vmcnt(6)
	v_lshl_add_u32 v6, v6, 14, v8
	v_and_b32_e32 v5, 1, v5
	v_bitop3_b32 v14, v12, s34, v4 bitop3:0xde
	v_bitop3_b32 v4, v12, s38, v4 bitop3:0xde
	s_cmpk_lt_u32 s0, 0x100
	v_lshl_or_b32 v5, v5, 6, v6
	v_readlane_b32 s38, v254, 21
	v_lshl_or_b32 v226, s78, 5, v13
	s_cselect_b64 s[46:47], -1, 0
	s_mov_b32 s0, 0
	v_mov_b32_e32 v207, v3
	v_lshl_add_u32 v208, v7, 1, v5
	v_mov_b32_e32 v209, v3
	v_add_u32_e32 v227, 0, v4
	v_add_u32_e32 v228, 0, v14
	s_mov_b32 s34, s101
	s_mov_b32 s95, s100
	s_barrier
	v_readlane_b32 s39, v254, 22
	s_branch .LBB0_1220
